# M1 K-loop: the post-MFMA s_barrier of each sub-phase moved ahead of the last MFMA (skip path keeps its own barrier)
# baseline (speedup 1.0000x reference)
;     ...
;         for (int t = 0; t < nt; t += 2) {
;             const bool last = (t == nt - 2);
;             const int t1 = kmod ? (t + 1) % kmod : t + 1, t2 = kmod ? (t + 2) % kmod : t + 2;
;             const char* a1 = cA + (size_t)t1 * kstep;
;             const char* a2 = last ? nA : cA + (size_t)t2 * kstep; const char* b2 = last ? nB : cB + (size_t)t2 * kstep;
;             const char* a3 = a2 + kstep; const char* b3 = b2 + kstep;
.Leb4_join:
	s_add_i32 s3, s3, 2
	s_add_u32 s34, s34, 0x100
	s_addc_u32 s35, s35, 0
	s_cmp_gt_u32 s3, 5
	s_cbranch_scc1 .LBB0_1230

; #define PG8_WAIT_V(n) asm volatile("s_waitcnt vmcnt(" #n ")" ::: "memory")
; #define PG8_WAIT_L(n) asm volatile("s_waitcnt lgkmcnt(" #n ")" ::: "memory")
; #define PG8_BAR __builtin_amdgcn_s_barrier()
; #define PG8_SCHED __builtin_amdgcn_sched_barrier(0)
;     ...
;             PG8_WAIT_V(8); PG8_WAIT_L(0); PG8_BAR; if (cur.half != 2) { PG8_MMA(0, 0, At, B0); PG8_MMA(0, 1, At, B1); } PG8_BAR; PG8_SCHED;
.LBB0_1222:
	s_waitcnt vmcnt(8)
	s_waitcnt lgkmcnt(0)
	v_cndmask_b32_e64 v0, 0, 1, s[28:29]
	v_cmp_ne_u32_e64 s[6:7], 1, v0
	s_andn2_b64 vcc, exec, s[28:29]
	s_barrier
	s_cbranch_vccnz .Leb1_skip
	s_setprio 1
	s_waitcnt lgkmcnt(0)
	v_mfma_f32_16x16x128_f8f6f4 v[190:193], v[18:25], v[58:65], v[190:193]
	v_mfma_f32_16x16x128_f8f6f4 v[186:189], v[26:33], v[58:65], v[186:189]
	v_mfma_f32_16x16x128_f8f6f4 v[174:177], v[18:25], v[50:57], v[174:177]
	v_mfma_f32_16x16x128_f8f6f4 v[170:173], v[26:33], v[50:57], v[170:173]
	v_mfma_f32_16x16x128_f8f6f4 v[158:161], v[18:25], v[42:49], v[158:161]
	v_mfma_f32_16x16x128_f8f6f4 v[154:157], v[26:33], v[42:49], v[154:157]
	v_mfma_f32_16x16x128_f8f6f4 v[142:145], v[18:25], v[34:41], v[142:145]
	v_mfma_f32_16x16x128_f8f6f4 v[138:141], v[26:33], v[34:41], v[138:141]
	s_setprio 0
	s_setprio 1
	v_mfma_f32_16x16x128_f8f6f4 v[182:185], v[2:9], v[58:65], v[182:185]
	v_mfma_f32_16x16x128_f8f6f4 v[178:181], v[10:17], v[58:65], v[178:181]
	v_mfma_f32_16x16x128_f8f6f4 v[166:169], v[2:9], v[50:57], v[166:169]
	v_mfma_f32_16x16x128_f8f6f4 v[162:165], v[10:17], v[50:57], v[162:165]
	v_mfma_f32_16x16x128_f8f6f4 v[150:153], v[2:9], v[42:49], v[150:153]
	v_mfma_f32_16x16x128_f8f6f4 v[146:149], v[10:17], v[42:49], v[146:149]
	v_mfma_f32_16x16x128_f8f6f4 v[134:137], v[2:9], v[34:41], v[134:137]
	s_barrier
	v_mfma_f32_16x16x128_f8f6f4 v[130:133], v[10:17], v[34:41], v[130:133]
	s_setprio 0
	s_branch .Leb1_join

; #define PG8_STAGE_B(bufoff, gbase) PG8_STAGE_U(bufoff, gbase, voffB, qstepB)
; #define PG8_STAGE_A(bufoff, gbase, h, GO) do { if constexpr (GATHER) { PG8_STAGE(bufoff, gbase, (GO)[h]); } else { PG8_STAGE_U(bufoff, (const char*)(gbase) + (h) * hstepA, voffA, qstepA); } } while (0)
; #define PG8_LDA(dst, b, h) do { _Pragma("unroll") for (int m = 0; m < 4; ++m) _Pragma("unroll") for (int k = 0; k < 2; ++k) dst[m][k] = *(const LAS bf16x8*)(lds + PG8_SA(b, h) + aoff + m * 2048 + k * 1024); } while (0)
; #define PG8_LDB(dst, b, h) do { _Pragma("unroll") for (int n = 0; n < 2; ++n) _Pragma("unroll") for (int k = 0; k < 2; ++k) dst[n][k] = *(const LAS bf16x8*)(lds + PG8_SB(b, h) + boff + n * 2048 + k * 1024); } while (0)
; #define PG8_WAIT_V(n) asm volatile("s_waitcnt vmcnt(" #n ")" ::: "memory")
; #define PG8_BAR __builtin_amdgcn_s_barrier()
;     ...
;             const int t1 = kmod ? (t + 1) % kmod : t + 1, t2 = kmod ? (t + 2) % kmod : t + 2;
;             const char* a1 = cA + (size_t)t1 * kstep;
;             const char* a2 = last ? nA : cA + (size_t)t2 * kstep; const char* b2 = last ? nB : cB + (size_t)t2 * kstep;
;             const char* a3 = a2 + kstep; const char* b3 = b2 + kstep;
;             if constexpr (MidT<Epi>::v >= 0) { if (t == MidT<Epi>::v) { unsigned o2 = ~0u; int w2 = wave_s; asm volatile("" : "+s"(w2), "+s"(o2)); int l2 = (int)__builtin_amdgcn_mbcnt_hi(o2, __builtin_amdgcn_mbcnt_lo(o2, 0u)); asm volatile("" : "+v"(l2));
;                 E.mid(acc, cur, w2 >> 2, w2 & 3, l2 & 15, l2 >> 4); } }
;             PG8_LDB(B0, 0, 0); PG8_LDB(B1, 0, 1); PG8_SCHED; PG8_LDA(At, 0, 0); PG8_STAGE_A(PG8_SA(1, 1), a1, 1, gc);
;             if constexpr (GATHER) { if (last && has_next) {
; #pragma unroll
;                 for (int h = 0; h < 2; ++h)
; #pragma unroll
;                     for (int i = 0; i < 2; ++i) { int _R, _C; stage_rc(tid * 16 + i * 8192, _R, _C); gc[h][i] = gn[h][i] * (unsigned)(lda * 2) + (unsigned)(_C * 2); } } }
;             PG8_WAIT_V(8); PG8_WAIT_L(0); PG8_BAR; if (cur.half != 2) { PG8_MMA(0, 0, At, B0); PG8_MMA(0, 1, At, B1); } PG8_BAR; PG8_SCHED;
;             PG8_LDA(At, 0, 1); PG8_STAGE_B(PG8_SB(0, 0), b2); PG8_STAGE_B(PG8_SB(0, 1), b2 + hstepB); PG8_STAGE_A(PG8_SA(0, 0), a2, 0, gc);
;             PG8_WAIT_V(8); PG8_WAIT_L(0); PG8_BAR; if (cur.half != 1) { PG8_MMA(1, 0, At, B0); PG8_MMA(1, 1, At, B1); } PG8_BAR; PG8_SCHED;
.Leb1_join:
.LBB0_1224:
	s_add_u32 s36, s10, s34
	s_addc_u32 s37, s11, s35
	s_add_u32 s42, s36, 0x100
	s_addc_u32 s43, s37, 0
	s_and_b64 s[36:37], s[8:9], exec
	s_cselect_b32 s37, s17, s43
	s_cselect_b32 s36, s25, s42
	s_add_u32 s42, s0, s34
	s_addc_u32 s43, s1, s35
	s_and_b64 s[8:9], s[8:9], exec
	s_cselect_b32 s43, s48, s43
	s_cselect_b32 s42, s49, s42
	v_mov_b32_e32 v0, v217
	s_mov_b32 m0, s78
	s_waitcnt lgkmcnt(0)
	ds_read_b128 v[58:61], v224 offset:16384
	ds_read_b128 v[62:65], v224 offset:17408
	ds_read_b128 v[50:53], v224 offset:18432
	ds_read_b128 v[54:57], v224 offset:19456
	ds_read_b128 v[42:45], v224 offset:20480
	ds_read_b128 v[46:49], v224 offset:21504
	ds_read_b128 v[34:37], v224 offset:22528
	ds_read_b128 v[38:41], v224 offset:23552
	s_andn2_b64 vcc, exec, s[22:23]
	global_load_lds_dwordx4 v0, s[42:43]
	v_mov_b32_e32 v0, v217
	s_mov_b32 m0, s79
	v_lshl_add_u64 v[194:195], s[42:43], 0, v[0:1]
	v_lshl_add_u64 v[194:195], v[194:195], 0, s[74:75]
	v_mov_b32_e32 v0, v217
	global_load_lds_dwordx4 v[194:195], off
	s_mov_b32 m0, s95
	v_lshl_add_u64 v[194:195], s[42:43], 0, v[0:1]
	v_lshl_add_u64 v[194:195], v[194:195], 0, s[80:81]
	v_mov_b32_e32 v0, v217
	global_load_lds_dwordx4 v[194:195], off
	s_mov_b32 m0, s39
	v_lshl_add_u64 v[194:195], s[42:43], 0, v[0:1]
	v_lshl_add_u64 v[194:195], v[194:195], 0, s[82:83]
	v_mov_b32_e32 v0, v218
	global_load_lds_dwordx4 v[194:195], off
	s_mov_b32 m0, s63
	s_nop 0
	global_load_lds_dwordx4 v0, s[36:37]
	v_mov_b32_e32 v0, v222
	s_mov_b32 m0, s33
	s_nop 0
	global_load_lds_dwordx4 v0, s[36:37]
	s_waitcnt vmcnt(8)
	s_waitcnt lgkmcnt(0)
	v_cndmask_b32_e64 v0, 0, 1, s[22:23]
	v_cmp_ne_u32_e64 s[8:9], 1, v0
	s_barrier
	s_cbranch_vccnz .Leb2_skip
	s_setprio 1
	s_waitcnt lgkmcnt(0)
	v_mfma_f32_16x16x128_f8f6f4 v[126:129], v[18:25], v[58:65], v[126:129]
	v_mfma_f32_16x16x128_f8f6f4 v[122:125], v[26:33], v[58:65], v[122:125]
	v_mfma_f32_16x16x128_f8f6f4 v[110:113], v[18:25], v[50:57], v[110:113]
	v_mfma_f32_16x16x128_f8f6f4 v[106:109], v[26:33], v[50:57], v[106:109]
	v_mfma_f32_16x16x128_f8f6f4 v[94:97], v[18:25], v[42:49], v[94:97]
	v_mfma_f32_16x16x128_f8f6f4 v[90:93], v[26:33], v[42:49], v[90:93]
	v_mfma_f32_16x16x128_f8f6f4 v[78:81], v[18:25], v[34:41], v[78:81]
	v_mfma_f32_16x16x128_f8f6f4 v[74:77], v[26:33], v[34:41], v[74:77]
	s_setprio 0
	s_setprio 1
	v_mfma_f32_16x16x128_f8f6f4 v[118:121], v[2:9], v[58:65], v[118:121]
	v_mfma_f32_16x16x128_f8f6f4 v[114:117], v[10:17], v[58:65], v[114:117]
	v_mfma_f32_16x16x128_f8f6f4 v[102:105], v[2:9], v[50:57], v[102:105]
	v_mfma_f32_16x16x128_f8f6f4 v[98:101], v[10:17], v[50:57], v[98:101]
	v_mfma_f32_16x16x128_f8f6f4 v[86:89], v[2:9], v[42:49], v[86:89]
	v_mfma_f32_16x16x128_f8f6f4 v[82:85], v[10:17], v[42:49], v[82:85]
	v_mfma_f32_16x16x128_f8f6f4 v[70:73], v[2:9], v[34:41], v[70:73]
	s_barrier
	v_mfma_f32_16x16x128_f8f6f4 v[66:69], v[10:17], v[34:41], v[66:69]
	s_setprio 0
	s_branch .Leb2_join

; #define PG8_STAGE_A(bufoff, gbase, h, GO) do { if constexpr (GATHER) { PG8_STAGE(bufoff, gbase, (GO)[h]); } else { PG8_STAGE_U(bufoff, (const char*)(gbase) + (h) * hstepA, voffA, qstepA); } } while (0)
; #define PG8_LDA(dst, b, h) do { _Pragma("unroll") for (int m = 0; m < 4; ++m) _Pragma("unroll") for (int k = 0; k < 2; ++k) dst[m][k] = *(const LAS bf16x8*)(lds + PG8_SA(b, h) + aoff + m * 2048 + k * 1024); } while (0)
; #define PG8_LDB(dst, b, h) do { _Pragma("unroll") for (int n = 0; n < 2; ++n) _Pragma("unroll") for (int k = 0; k < 2; ++k) dst[n][k] = *(const LAS bf16x8*)(lds + PG8_SB(b, h) + boff + n * 2048 + k * 1024); } while (0)
; #define PG8_WAIT_V(n) asm volatile("s_waitcnt vmcnt(" #n ")" ::: "memory")
; #define PG8_WAIT_L(n) asm volatile("s_waitcnt lgkmcnt(" #n ")" ::: "memory")
; #define PG8_BAR __builtin_amdgcn_s_barrier()
; #define PG8_SCHED __builtin_amdgcn_sched_barrier(0)
;     ...
;             PG8_LDB(B0, 1, 0); PG8_LDB(B1, 1, 1); PG8_SCHED; PG8_LDA(At, 1, 0); PG8_STAGE_A(PG8_SA(0, 1), a2, 1, gc);
;             PG8_WAIT_V(8); PG8_WAIT_L(0); PG8_BAR; if (cur.half != 2) { PG8_MMA(0, 0, At, B0); PG8_MMA(0, 1, At, B1); } PG8_BAR; PG8_SCHED;
.Leb2_join:
.LBB0_1226:
	v_add_u32_e32 v0, 0x18000, v223
	ds_read_b128 v[18:21], v0
	ds_read_b128 v[22:25], v0 offset:1024
	ds_read_b128 v[26:29], v0 offset:2048
	ds_read_b128 v[30:33], v0 offset:3072
	v_add_u32_e32 v0, 0x1c000, v223
	ds_read_b128 v[2:5], v0
	ds_read_b128 v[6:9], v0 offset:1024
	ds_read_b128 v[10:13], v0 offset:2048
	ds_read_b128 v[14:17], v0 offset:3072
	v_mov_b32_e32 v0, v221
	s_mov_b32 m0, s76
	s_waitcnt lgkmcnt(0)
	ds_read_b128 v[58:61], v224 offset:32768
	ds_read_b128 v[62:65], v224 offset:33792
	ds_read_b128 v[50:53], v224 offset:34816
	ds_read_b128 v[54:57], v224 offset:35840
	ds_read_b128 v[42:45], v224 offset:36864
	ds_read_b128 v[46:49], v224 offset:37888
	ds_read_b128 v[34:37], v224 offset:38912
	ds_read_b128 v[38:41], v224 offset:39936
	s_and_b64 vcc, exec, s[6:7]
	global_load_lds_dwordx4 v0, s[36:37]
	v_mov_b32_e32 v0, v220
	s_mov_b32 m0, s77
	s_nop 0
	global_load_lds_dwordx4 v0, s[36:37]
	s_waitcnt vmcnt(8)
	s_waitcnt lgkmcnt(0)
	s_barrier
	s_cbranch_vccnz .Leb3_skip
	s_setprio 1
	s_waitcnt lgkmcnt(0)
	v_mfma_f32_16x16x128_f8f6f4 v[190:193], v[18:25], v[58:65], v[190:193]
	v_mfma_f32_16x16x128_f8f6f4 v[186:189], v[26:33], v[58:65], v[186:189]
	v_mfma_f32_16x16x128_f8f6f4 v[174:177], v[18:25], v[50:57], v[174:177]
	v_mfma_f32_16x16x128_f8f6f4 v[170:173], v[26:33], v[50:57], v[170:173]
	v_mfma_f32_16x16x128_f8f6f4 v[158:161], v[18:25], v[42:49], v[158:161]
	v_mfma_f32_16x16x128_f8f6f4 v[154:157], v[26:33], v[42:49], v[154:157]
	v_mfma_f32_16x16x128_f8f6f4 v[142:145], v[18:25], v[34:41], v[142:145]
	v_mfma_f32_16x16x128_f8f6f4 v[138:141], v[26:33], v[34:41], v[138:141]
	s_setprio 0
	s_setprio 1
	v_mfma_f32_16x16x128_f8f6f4 v[182:185], v[2:9], v[58:65], v[182:185]
	v_mfma_f32_16x16x128_f8f6f4 v[178:181], v[10:17], v[58:65], v[178:181]
	v_mfma_f32_16x16x128_f8f6f4 v[166:169], v[2:9], v[50:57], v[166:169]
	v_mfma_f32_16x16x128_f8f6f4 v[162:165], v[10:17], v[50:57], v[162:165]
	v_mfma_f32_16x16x128_f8f6f4 v[150:153], v[2:9], v[42:49], v[150:153]
	v_mfma_f32_16x16x128_f8f6f4 v[146:149], v[10:17], v[42:49], v[146:149]
	v_mfma_f32_16x16x128_f8f6f4 v[134:137], v[2:9], v[34:41], v[134:137]
	s_barrier
	v_mfma_f32_16x16x128_f8f6f4 v[130:133], v[10:17], v[34:41], v[130:133]
	s_setprio 0
	s_branch .Leb3_join

; #define PG8_STAGE_B(bufoff, gbase) PG8_STAGE_U(bufoff, gbase, voffB, qstepB)
; #define PG8_STAGE_A(bufoff, gbase, h, GO) do { if constexpr (GATHER) { PG8_STAGE(bufoff, gbase, (GO)[h]); } else { PG8_STAGE_U(bufoff, (const char*)(gbase) + (h) * hstepA, voffA, qstepA); } } while (0)
; #define PG8_LDA(dst, b, h) do { _Pragma("unroll") for (int m = 0; m < 4; ++m) _Pragma("unroll") for (int k = 0; k < 2; ++k) dst[m][k] = *(const LAS bf16x8*)(lds + PG8_SA(b, h) + aoff + m * 2048 + k * 1024); } while (0)
; #define PG8_WAIT_V(n) asm volatile("s_waitcnt vmcnt(" #n ")" ::: "memory")
; #define PG8_WAIT_L(n) asm volatile("s_waitcnt lgkmcnt(" #n ")" ::: "memory")
; #define PG8_BAR __builtin_amdgcn_s_barrier()
; #define PG8_SCHED __builtin_amdgcn_sched_barrier(0)
;     ...
;             PG8_LDA(At, 1, 1); PG8_STAGE_B(PG8_SB(1, 0), b3); PG8_STAGE_B(PG8_SB(1, 1), b3 + hstepB); PG8_STAGE_A(PG8_SA(1, 0), a3, 0, gc);
;             PG8_WAIT_V(8); PG8_WAIT_L(0); PG8_BAR; if (cur.half != 1) { PG8_MMA(1, 0, At, B0); PG8_MMA(1, 1, At, B1); } PG8_BAR; PG8_SCHED;
.Leb3_join:
.LBB0_1228:
	v_mov_b32_e32 v0, v217
	s_waitcnt lgkmcnt(0)
	ds_read_b128 v[58:61], v224 offset:49152
	ds_read_b128 v[62:65], v224 offset:50176
	ds_read_b128 v[50:53], v224 offset:51200
	ds_read_b128 v[54:57], v224 offset:52224
	ds_read_b128 v[42:45], v224 offset:53248
	ds_read_b128 v[46:49], v224 offset:54272
	ds_read_b128 v[34:37], v224 offset:55296
	ds_read_b128 v[38:41], v224 offset:56320
	s_mov_b32 m0, s51
	v_lshl_add_u64 v[194:195], s[42:43], 0, v[0:1]
	v_lshl_add_u64 v[194:195], v[194:195], 0, s[84:85]
	v_mov_b32_e32 v0, v217
	global_load_lds_dwordx4 v[194:195], off
	s_mov_b32 m0, s38
	v_lshl_add_u64 v[194:195], s[42:43], 0, v[0:1]
	v_lshl_add_u64 v[194:195], v[194:195], 0, s[86:87]
	v_mov_b32_e32 v0, v217
	global_load_lds_dwordx4 v[194:195], off
	s_mov_b32 m0, s94
	v_lshl_add_u64 v[194:195], s[42:43], 0, v[0:1]
	v_lshl_add_u64 v[194:195], v[194:195], 0, s[88:89]
	v_mov_b32_e32 v0, v217
	global_load_lds_dwordx4 v[194:195], off
	s_mov_b32 m0, s71
	v_lshl_add_u64 v[194:195], s[42:43], 0, v[0:1]
	v_lshl_add_u64 v[194:195], v[194:195], 0, s[90:91]
	v_mov_b32_e32 v0, v218
	global_load_lds_dwordx4 v[194:195], off
	s_mov_b32 m0, s44
	v_lshl_add_u64 v[194:195], s[36:37], 0, v[0:1]
	v_lshl_add_u64 v[194:195], v[194:195], 0, s[84:85]
	v_mov_b32_e32 v0, v222
	global_load_lds_dwordx4 v[194:195], off
	s_mov_b32 m0, s70
	v_lshl_add_u64 v[194:195], s[36:37], 0, v[0:1]
	v_lshl_add_u64 v[194:195], v[194:195], 0, s[84:85]
	global_load_lds_dwordx4 v[194:195], off
	s_waitcnt vmcnt(8)
	s_waitcnt lgkmcnt(0)
	s_and_b64 vcc, exec, s[8:9]
	s_barrier
	s_cbranch_vccnz .LBB0_1216
	s_setprio 1
	s_waitcnt lgkmcnt(0)
	v_mfma_f32_16x16x128_f8f6f4 v[126:129], v[18:25], v[58:65], v[126:129]
	v_mfma_f32_16x16x128_f8f6f4 v[122:125], v[26:33], v[58:65], v[122:125]
	v_mfma_f32_16x16x128_f8f6f4 v[110:113], v[18:25], v[50:57], v[110:113]
	v_mfma_f32_16x16x128_f8f6f4 v[106:109], v[26:33], v[50:57], v[106:109]
	v_mfma_f32_16x16x128_f8f6f4 v[94:97], v[18:25], v[42:49], v[94:97]
	v_mfma_f32_16x16x128_f8f6f4 v[90:93], v[26:33], v[42:49], v[90:93]
	v_mfma_f32_16x16x128_f8f6f4 v[78:81], v[18:25], v[34:41], v[78:81]
	v_mfma_f32_16x16x128_f8f6f4 v[74:77], v[26:33], v[34:41], v[74:77]
	s_setprio 0
	s_setprio 1
	v_mfma_f32_16x16x128_f8f6f4 v[118:121], v[2:9], v[58:65], v[118:121]
	v_mfma_f32_16x16x128_f8f6f4 v[114:117], v[10:17], v[58:65], v[114:117]
	v_mfma_f32_16x16x128_f8f6f4 v[102:105], v[2:9], v[50:57], v[102:105]
	v_mfma_f32_16x16x128_f8f6f4 v[98:101], v[10:17], v[50:57], v[98:101]
	v_mfma_f32_16x16x128_f8f6f4 v[86:89], v[2:9], v[42:49], v[86:89]
	v_mfma_f32_16x16x128_f8f6f4 v[82:85], v[10:17], v[42:49], v[82:85]
	v_mfma_f32_16x16x128_f8f6f4 v[70:73], v[2:9], v[34:41], v[70:73]
	s_barrier
	v_mfma_f32_16x16x128_f8f6f4 v[66:69], v[10:17], v[34:41], v[66:69]
	s_setprio 0
	s_branch .Leb4_join

; __global__ void __launch_bounds__(512, 2) fwd_kernel(Args args) {
	.amdhsa_kernel _Z10fwd_kernel4Args
		.amdhsa_group_segment_fixed_size 0
		.amdhsa_private_segment_fixed_size 0
		.amdhsa_kernarg_size 496
		.amdhsa_user_sgpr_count 2
		.amdhsa_user_sgpr_dispatch_ptr 0
		.amdhsa_user_sgpr_queue_ptr 0
		.amdhsa_user_sgpr_kernarg_segment_ptr 1
		.amdhsa_user_sgpr_dispatch_id 0
		.amdhsa_user_sgpr_kernarg_preload_length 0
		.amdhsa_user_sgpr_kernarg_preload_offset 0
		.amdhsa_user_sgpr_private_segment_size 0
		.amdhsa_uses_dynamic_stack 0
		.amdhsa_enable_private_segment 0
		.amdhsa_system_sgpr_workgroup_id_x 1
		.amdhsa_system_sgpr_workgroup_id_y 0
		.amdhsa_system_sgpr_workgroup_id_z 0
		.amdhsa_system_sgpr_workgroup_info 0
		.amdhsa_system_vgpr_workitem_id 0
		.amdhsa_next_free_vgpr 256
		.amdhsa_next_free_sgpr 100
		.amdhsa_accum_offset 256
		.amdhsa_reserve_vcc 1
		.amdhsa_float_round_mode_32 0
		.amdhsa_float_round_mode_16_64 0
		.amdhsa_float_denorm_mode_32 3
		.amdhsa_float_denorm_mode_16_64 3
		.amdhsa_dx10_clamp 1
		.amdhsa_ieee_mode 1
		.amdhsa_fp16_overflow 0
		.amdhsa_tg_split 0
		.amdhsa_exception_fp_ieee_invalid_op 0
		.amdhsa_exception_fp_denorm_src 0
		.amdhsa_exception_fp_ieee_div_zero 0
		.amdhsa_exception_fp_ieee_overflow 0
		.amdhsa_exception_fp_ieee_underflow 0
		.amdhsa_exception_fp_ieee_inexact 0
		.amdhsa_exception_int_div_zero 0
	.end_amdhsa_kernel

; __global__ void __launch_bounds__(512, 2) fwd_kernel(Args args) {
amdhsa.kernels:
  - .agpr_count:     0
    .args:
      - .offset:         0
        .size:           240
        .value_kind:     by_value
      - .offset:         240
        .size:           4
        .value_kind:     hidden_block_count_x
      - .offset:         244
        .size:           4
        .value_kind:     hidden_block_count_y
      - .offset:         248
        .size:           4
        .value_kind:     hidden_block_count_z
      - .offset:         252
        .size:           2
        .value_kind:     hidden_group_size_x
      - .offset:         254
        .size:           2
        .value_kind:     hidden_group_size_y
      - .offset:         256
        .size:           2
        .value_kind:     hidden_group_size_z
      - .offset:         258
        .size:           2
        .value_kind:     hidden_remainder_x
      - .offset:         260
        .size:           2
        .value_kind:     hidden_remainder_y
      - .offset:         262
        .size:           2
        .value_kind:     hidden_remainder_z
      - .offset:         280
        .size:           8
        .value_kind:     hidden_global_offset_x
      - .offset:         288
        .size:           8
        .value_kind:     hidden_global_offset_y
      - .offset:         296
        .size:           8
        .value_kind:     hidden_global_offset_z
      - .offset:         304
        .size:           2
        .value_kind:     hidden_grid_dims
      - .offset:         360
        .size:           4
        .value_kind:     hidden_dynamic_lds_size
    .group_segment_fixed_size: 0
    .kernarg_segment_align: 8
    .kernarg_segment_size: 496
    .language:       OpenCL C
    .language_version:
      - 2
      - 0
    .max_flat_workgroup_size: 512
    .name:           _Z10fwd_kernel4Args
    .private_segment_fixed_size: 0
    .sgpr_count:     106
    .sgpr_spill_count: 175
    .symbol:         _Z10fwd_kernel4Args.kd
    .uniform_work_group_size: 1
    .uses_dynamic_stack: false
    .vgpr_count:     256
    .vgpr_spill_count: 0
    .wavefront_size: 64
